# P0: PB=bf16(p) loop with six trips of loads in flight; rmsnorm(x) row loop prefetches the next row into a second register set
# baseline (speedup 1.0000x reference)
; __device__ __forceinline__ unsigned cvt4_fp8(float a, float b, float c, float d) { int w = 0; w = __builtin_amdgcn_cvt_pk_fp8_f32(a, b, w, false); w = __builtin_amdgcn_cvt_pk_fp8_f32(c, d, w, true); return (unsigned)w; }
; __global__ void __launch_bounds__(512, 2) mega_fwd(Args args) {
;     ...
;           for (int m = gwc; m < T; m += NGWc) { const f32x4* xr = (const f32x4*)(x + (size_t)m * DM) + lane; f32x4 v[8]; float s = 0.f;
; #pragma unroll
;               for (int j = 0; j < 8; ++j) { v[j] = xr[64 * j]; s += (v[j][0] * v[j][0] + v[j][1] * v[j][1]) + (v[j][2] * v[j][2] + v[j][3] * v[j][3]); }
;               const float rstd = 1.0f / sqrtf(wave_sum(s) * (1.0f / DM) + EPS);
;               unsigned* o4 = (unsigned*)(XN8 + (size_t)m * DM) + lane;
; #pragma unroll
;               for (int j = 0; j < 8; ++j) { const f32x4 gv = ((const f32x4*)gn)[64 * j + lane]; o4[64 * j] = cvt4_fp8(v[j][0] * rstd * gv[0], v[j][1] * rstd * gv[1], v[j][2] * rstd * gv[2], v[j][3] * rstd * gv[3]); } } }
.LBB0_1091:
	s_or_b64 exec, exec, s[4:5]
	s_load_dwordx4 s[8:11], s[0:1], 0x8
	s_load_dwordx2 s[46:47], s[0:1], 0x68
	s_cmpk_gt_i32 s42, 0x3fff
	s_cbranch_scc1 .LBB0_1094
	v_mbcnt_lo_u32_b32 v2, -1, 0
	v_mbcnt_hi_u32_b32 v2, -1, v2
	v_and_b32_e32 v3, 64, v2
	v_add_u32_e32 v3, 64, v3
	v_xor_b32_e32 v4, 1, v2
	v_cmp_lt_i32_e32 vcc, v4, v3
	s_load_dwordx2 s[16:17], s[0:1], 0x0
	s_ashr_i32 s43, s42, 31
	v_cndmask_b32_e32 v4, v2, v4, vcc
	v_lshlrev_b32_e32 v38, 2, v4
	v_xor_b32_e32 v4, 2, v2
	v_cmp_lt_i32_e32 vcc, v4, v3
	s_mov_b64 s[4:5], 0x1000
	v_mov_b32_e32 v44, 0x358637bd
	v_cndmask_b32_e32 v4, v2, v4, vcc
	v_lshlrev_b32_e32 v39, 2, v4
	v_xor_b32_e32 v4, 4, v2
	v_cmp_lt_i32_e32 vcc, v4, v3
	s_mov_b32 s3, 0xf800000
	v_mov_b32_e32 v45, 0x260
	v_cndmask_b32_e32 v4, v2, v4, vcc
	v_lshlrev_b32_e32 v40, 2, v4
	v_xor_b32_e32 v4, 8, v2
	v_cmp_lt_i32_e32 vcc, v4, v3
	s_nop 1
	v_cndmask_b32_e32 v4, v2, v4, vcc
	v_lshlrev_b32_e32 v41, 2, v4
	v_xor_b32_e32 v4, 16, v2
	v_cmp_lt_i32_e32 vcc, v4, v3
	s_nop 1
	v_cndmask_b32_e32 v4, v2, v4, vcc
	v_lshlrev_b32_e32 v42, 2, v4
	v_xor_b32_e32 v4, 32, v2
	v_cmp_lt_i32_e32 vcc, v4, v3
	v_mov_b32_e32 v3, 0
	s_nop 0
	v_cndmask_b32_e32 v2, v2, v4, vcc
	v_lshlrev_b32_e32 v43, 2, v2
	v_lshlrev_b32_e32 v2, 4, v164
	s_waitcnt lgkmcnt(0)
	v_lshl_add_u64 v[24:25], s[10:11], 0, v[2:3]
	s_mov_b64 s[10:11], 0x1400
	s_waitcnt vmcnt(0)
	v_lshl_add_u64 v[28:29], v[24:25], 0, s[10:11]
	s_mov_b64 s[10:11], 0x1800
	v_lshl_add_u64 v[30:31], v[24:25], 0, s[10:11]
	s_mov_b64 s[10:11], 0x1c00
	v_lshl_add_u64 v[32:33], v[24:25], 0, s[10:11]
	s_lshl_b64 s[10:11], s[42:43], 13
	s_add_u32 s10, s16, s10
	s_addc_u32 s11, s17, s11
	v_lshl_add_u64 v[4:5], s[10:11], 0, v[2:3]
	s_ashr_i32 s45, s44, 31
	v_lshl_add_u64 v[26:27], v[24:25], 0, s[4:5]
	v_lshl_add_u64 v[34:35], v[4:5], 0, s[4:5]
	s_lshl_b64 s[10:11], s[44:45], 13
	s_lshl_b64 s[4:5], s[42:43], 11
	s_add_u32 s4, s18, s4
	v_lshlrev_b32_e32 v2, 2, v164
	s_addc_u32 s5, s19, s5
	v_lshl_add_u64 v[2:3], s[4:5], 0, v[2:3]
	s_mov_b64 s[4:5], 0x25000000
	v_lshl_add_u64 v[36:37], v[2:3], 0, s[4:5]
	s_lshl_b64 s[48:49], s[44:45], 11
	global_load_dwordx4 v[200:203], v[24:25], off offset:1024
	global_load_dwordx4 v[204:207], v[24:25], off offset:2048
	global_load_dwordx4 v[208:211], v[24:25], off offset:3072
	global_load_dwordx4 v[212:215], v[26:27], off
	global_load_dwordx4 v[216:219], v[28:29], off
	global_load_dwordx4 v[220:223], v[30:31], off
	global_load_dwordx4 v[224:227], v[32:33], off
	s_waitcnt vmcnt(0)
	global_load_dwordx4 v[148:151], v[34:35], off offset:-4096
	global_load_dwordx4 v[152:155], v[34:35], off offset:-3072
	global_load_dwordx4 v[156:159], v[34:35], off offset:-2048
	global_load_dwordx4 v[182:185], v[34:35], off offset:-1024
	global_load_dwordx4 v[186:189], v[34:35], off
	global_load_dwordx4 v[190:193], v[34:35], off offset:1024
	global_load_dwordx4 v[194:197], v[34:35], off offset:2048
	global_load_dwordx4 v[236:239], v[34:35], off offset:3072
	s_waitcnt vmcnt(0)
.LBB0_1093:
	s_waitcnt vmcnt(8)
	v_mov_b32_e32 v46, v148
	v_mov_b32_e32 v47, v149
	v_mov_b32_e32 v48, v150
	v_mov_b32_e32 v49, v151
	v_mov_b32_e32 v50, v152
	v_mov_b32_e32 v51, v153
	v_mov_b32_e32 v52, v154
	v_mov_b32_e32 v53, v155
	v_mov_b32_e32 v54, v156
	v_mov_b32_e32 v55, v157
	v_mov_b32_e32 v56, v158
	v_mov_b32_e32 v57, v159
	v_mov_b32_e32 v18, v182
	v_mov_b32_e32 v19, v183
	v_mov_b32_e32 v20, v184
	v_mov_b32_e32 v21, v185
	v_mov_b32_e32 v14, v186
	v_mov_b32_e32 v15, v187
	v_mov_b32_e32 v16, v188
	v_mov_b32_e32 v17, v189
	v_mov_b32_e32 v10, v190
	v_mov_b32_e32 v11, v191
	v_mov_b32_e32 v12, v192
	v_mov_b32_e32 v13, v193
	v_mov_b32_e32 v6, v194
	v_mov_b32_e32 v7, v195
	v_mov_b32_e32 v8, v196
	v_mov_b32_e32 v9, v197
	v_mov_b32_e32 v2, v236
	v_mov_b32_e32 v3, v237
	v_mov_b32_e32 v4, v238
	v_mov_b32_e32 v5, v239
	global_load_dwordx4 v[58:61], v[24:25], off
	v_mov_b32_e32 v62, 0
	s_add_i32 s42, s42, s44
	s_cmpk_gt_i32 s42, 0x3fff
	s_cselect_b64 s[98:99], 0, s[10:11]
	v_lshl_add_u64 v[34:35], v[34:35], 0, s[98:99]
	global_load_dwordx4 v[148:151], v[34:35], off offset:-4096
	global_load_dwordx4 v[152:155], v[34:35], off offset:-3072
	global_load_dwordx4 v[156:159], v[34:35], off offset:-2048
	global_load_dwordx4 v[182:185], v[34:35], off offset:-1024
	global_load_dwordx4 v[186:189], v[34:35], off
	global_load_dwordx4 v[190:193], v[34:35], off offset:1024
	global_load_dwordx4 v[194:197], v[34:35], off offset:2048
	global_load_dwordx4 v[236:239], v[34:35], off offset:3072
	v_mul_f32_e32 v63, v47, v47
	v_mul_f32_e32 v64, v49, v49
	v_mul_f32_e32 v65, v51, v51
	v_mul_f32_e32 v66, v53, v53
	v_mul_f32_e32 v67, v55, v55
	v_mul_f32_e32 v68, v57, v57
	v_fmac_f32_e32 v63, v46, v46
	v_fmac_f32_e32 v64, v48, v48
	v_fmac_f32_e32 v65, v50, v50
	v_fmac_f32_e32 v66, v52, v52
	v_mul_f32_e32 v69, v19, v19
	v_mul_f32_e32 v70, v21, v21
	v_fmac_f32_e32 v67, v54, v54
	v_fmac_f32_e32 v68, v56, v56
	v_add_f32_e32 v63, v63, v64
	v_add_f32_e32 v64, v65, v66
	v_mul_f32_e32 v71, v15, v15
	v_mul_f32_e32 v72, v17, v17
	v_fmac_f32_e32 v69, v18, v18
	v_fmac_f32_e32 v70, v20, v20
	v_add_f32_e32 v65, v67, v68
	v_add_f32_e32 v63, v63, v64
	v_mul_f32_e32 v73, v11, v11
	v_mul_f32_e32 v74, v13, v13
	v_fmac_f32_e32 v71, v14, v14
	v_fmac_f32_e32 v72, v16, v16
	v_add_f32_e32 v66, v69, v70
	v_add_f32_e32 v63, v63, v65
	v_mul_f32_e32 v75, v7, v7
	v_mul_f32_e32 v76, v9, v9
	v_fmac_f32_e32 v73, v10, v10
	v_fmac_f32_e32 v74, v12, v12
	v_add_f32_e32 v67, v71, v72
	v_add_f32_e32 v63, v63, v66
	v_mul_f32_e32 v77, v3, v3
	v_mul_f32_e32 v78, v5, v5
	v_fmac_f32_e32 v75, v6, v6
	v_fmac_f32_e32 v76, v8, v8
	v_add_f32_e32 v68, v73, v74
	v_add_f32_e32 v63, v63, v67
	v_fmac_f32_e32 v77, v2, v2
	v_fmac_f32_e32 v78, v4, v4
	v_add_f32_e32 v69, v75, v76
	v_add_f32_e32 v63, v63, v68
	v_add_f32_e32 v70, v77, v78
	v_add_f32_e32 v63, v63, v69
	v_add_f32_e32 v63, v63, v70
	ds_bpermute_b32 v64, v38, v63
	s_waitcnt lgkmcnt(0)
; __device__ __forceinline__ unsigned cvt4_fp8(float a, float b, float c, float d) { int w = 0; w = __builtin_amdgcn_cvt_pk_fp8_f32(a, b, w, false); w = __builtin_amdgcn_cvt_pk_fp8_f32(c, d, w, true); return (unsigned)w; }
; __global__ void __launch_bounds__(512, 2) mega_fwd(Args args) {
;     ...
;               const float rstd = 1.0f / sqrtf(wave_sum(s) * (1.0f / DM) + EPS);
;               unsigned* o4 = (unsigned*)(XN8 + (size_t)m * DM) + lane;
; #pragma unroll
;               for (int j = 0; j < 8; ++j) { const f32x4 gv = ((const f32x4*)gn)[64 * j + lane]; o4[64 * j] = cvt4_fp8(v[j][0] * rstd * gv[0], v[j][1] * rstd * gv[1], v[j][2] * rstd * gv[2], v[j][3] * rstd * gv[3]); } } }
	v_add_f32_e32 v63, v63, v64
	ds_bpermute_b32 v64, v39, v63
	s_waitcnt lgkmcnt(0)
	v_add_f32_e32 v63, v63, v64
	ds_bpermute_b32 v64, v40, v63
	s_waitcnt lgkmcnt(0)
	v_add_f32_e32 v63, v63, v64
	ds_bpermute_b32 v64, v41, v63
	s_waitcnt lgkmcnt(0)
	v_add_f32_e32 v63, v63, v64
	ds_bpermute_b32 v64, v42, v63
	s_waitcnt lgkmcnt(0)
	v_add_f32_e32 v63, v63, v64
	ds_bpermute_b32 v64, v43, v63
	s_waitcnt lgkmcnt(0)
	v_add_f32_e32 v63, v63, v64
	v_fmamk_f32 v63, v63, 0x3a000000, v44
	v_mul_f32_e32 v64, 0x4f800000, v63
	v_cmp_gt_f32_e32 vcc, s3, v63
	s_nop 1
	v_cndmask_b32_e32 v63, v63, v64, vcc
	v_sqrt_f32_e32 v64, v63
	s_nop 0
	v_add_u32_e32 v65, -1, v64
	v_add_u32_e32 v66, 1, v64
	v_fma_f32 v67, -v65, v64, v63
	v_fma_f32 v68, -v66, v64, v63
	v_cmp_ge_f32_e64 s[4:5], 0, v67
	s_nop 1
	v_cndmask_b32_e64 v64, v64, v65, s[4:5]
	v_cmp_lt_f32_e64 s[4:5], 0, v68
	s_nop 1
	v_cndmask_b32_e64 v64, v64, v66, s[4:5]
	v_mul_f32_e32 v65, 0x37800000, v64
	v_cndmask_b32_e32 v64, v64, v65, vcc
	v_cmp_class_f32_e32 vcc, v63, v45
	s_nop 1
	v_cndmask_b32_e32 v63, v64, v63, vcc
	v_div_scale_f32 v64, s[4:5], v63, v63, 1.0
	v_rcp_f32_e32 v66, v64
	v_div_scale_f32 v65, vcc, 1.0, v63, 1.0
	v_fma_f32 v67, -v64, v66, 1.0
	v_fmac_f32_e32 v66, v67, v66
	v_mul_f32_e32 v67, v65, v66
	v_fma_f32 v68, -v64, v67, v65
	v_fmac_f32_e32 v67, v68, v66
	v_fma_f32 v64, -v64, v67, v65
	v_div_fmas_f32 v64, v64, v66, v67
	v_div_fixup_f32 v63, v64, v63, 1.0
	v_mul_f32_e32 v46, v63, v46
	v_mul_f32_e32 v47, v63, v47
	s_waitcnt vmcnt(8)
	v_mul_f32_e32 v46, v58, v46
	v_mul_f32_e32 v47, v59, v47
	v_cvt_pk_fp8_f32 v62, v46, v47
	v_mul_f32_e32 v48, v63, v48
	v_mul_f32_e32 v49, v63, v49
	v_mul_f32_e32 v48, v60, v48
	v_mul_f32_e32 v49, v61, v49
	v_cvt_pk_fp8_f32 v62, v48, v49 op_sel:[0,0,1]
	v_mul_f32_e32 v50, v63, v50
	v_mul_f32_e32 v51, v63, v51
	v_mov_b32_e32 v58, 0
	global_store_dword v[36:37], v62, off
	v_mul_f32_e32 v52, v63, v52
	v_mul_f32_e32 v53, v63, v53
	v_mul_f32_e32 v18, v63, v18
	v_mul_f32_e32 v19, v63, v19
	v_mul_f32_e32 v20, v63, v20
	v_mul_f32_e32 v21, v63, v21
	v_mul_f32_e32 v14, v63, v14
	v_mul_f32_e32 v15, v63, v15
	v_mul_f32_e32 v16, v63, v16
	v_mul_f32_e32 v17, v63, v17
	v_mul_f32_e32 v10, v63, v10
	v_mul_f32_e32 v11, v63, v11
	v_mul_f32_e32 v12, v63, v12
	v_mul_f32_e32 v13, v63, v13
	v_mul_f32_e32 v6, v63, v6
	v_mul_f32_e32 v7, v63, v7
	v_mul_f32_e32 v8, v63, v8
	v_mul_f32_e32 v9, v63, v9
	v_mul_f32_e32 v2, v63, v2
	v_mul_f32_e32 v3, v63, v3
	v_mul_f32_e32 v4, v63, v4
	v_mul_f32_e32 v5, v63, v5
	v_mov_b32_e32 v46, v200
	v_mov_b32_e32 v47, v201
	v_mov_b32_e32 v48, v202
	v_mov_b32_e32 v49, v203
	v_mul_f32_e32 v46, v46, v50
	v_mul_f32_e32 v47, v47, v51
	v_cvt_pk_fp8_f32 v58, v46, v47
	v_mul_f32_e32 v48, v48, v52
	v_mul_f32_e32 v49, v49, v53
	v_mul_f32_e32 v51, v63, v54
	v_cvt_pk_fp8_f32 v58, v48, v49 op_sel:[0,0,1]
	v_mul_f32_e32 v52, v63, v55
	v_mov_b32_e32 v50, 0
	v_mul_f32_e32 v53, v63, v56
	global_store_dword v[36:37], v58, off offset:256
	v_mul_f32_e32 v54, v63, v57
	v_mov_b32_e32 v46, v204
	v_mov_b32_e32 v47, v205
	v_mov_b32_e32 v48, v206
	v_mov_b32_e32 v49, v207
	v_mul_f32_e32 v46, v46, v51
	v_mul_f32_e32 v47, v47, v52
	v_cvt_pk_fp8_f32 v50, v46, v47
	v_mul_f32_e32 v48, v48, v53
	v_mul_f32_e32 v49, v49, v54
	v_cvt_pk_fp8_f32 v50, v48, v49 op_sel:[0,0,1]
	global_store_dword v[36:37], v50, off offset:512
	v_mov_b32_e32 v50, 0
	v_mov_b32_e32 v46, v208
	v_mov_b32_e32 v47, v209
	v_mov_b32_e32 v48, v210
	v_mov_b32_e32 v49, v211
	v_mul_f32_e32 v18, v46, v18
	v_mul_f32_e32 v19, v47, v19
	v_cvt_pk_fp8_f32 v50, v18, v19
	v_mul_f32_e32 v20, v48, v20
	v_mul_f32_e32 v21, v49, v21
	v_mov_b32_e32 v46, 0
	v_cvt_pk_fp8_f32 v50, v20, v21 op_sel:[0,0,1]
	global_store_dword v[36:37], v50, off offset:768
	v_mov_b32_e32 v18, v212
	v_mov_b32_e32 v19, v213
	v_mov_b32_e32 v20, v214
	v_mov_b32_e32 v21, v215
	v_mul_f32_e32 v14, v18, v14
	v_mul_f32_e32 v15, v19, v15
	v_cvt_pk_fp8_f32 v46, v14, v15
	v_mul_f32_e32 v16, v20, v16
	v_mul_f32_e32 v17, v21, v17
	v_mov_b32_e32 v18, 0
	v_cvt_pk_fp8_f32 v46, v16, v17 op_sel:[0,0,1]
	global_store_dword v[36:37], v46, off offset:1024
	v_mov_b32_e32 v14, v216
	v_mov_b32_e32 v15, v217
	v_mov_b32_e32 v16, v218
	v_mov_b32_e32 v17, v219
	v_mul_f32_e32 v10, v14, v10
	v_mul_f32_e32 v11, v15, v11
	v_cvt_pk_fp8_f32 v18, v10, v11
	v_mul_f32_e32 v12, v16, v12
	v_mul_f32_e32 v13, v17, v13
	v_mov_b32_e32 v14, 0
	v_cvt_pk_fp8_f32 v18, v12, v13 op_sel:[0,0,1]
	global_store_dword v[36:37], v18, off offset:1280
	v_mov_b32_e32 v10, v220
	v_mov_b32_e32 v11, v221
	v_mov_b32_e32 v12, v222
	v_mov_b32_e32 v13, v223
	v_mul_f32_e32 v6, v10, v6
	v_mul_f32_e32 v7, v11, v7
	v_cvt_pk_fp8_f32 v14, v6, v7
	v_mul_f32_e32 v8, v12, v8
	v_mul_f32_e32 v6, v13, v9
	v_mov_b32_e32 v10, 0
	v_cvt_pk_fp8_f32 v14, v8, v6 op_sel:[0,0,1]
	global_store_dword v[36:37], v14, off offset:1536
	v_mov_b32_e32 v6, v224
	v_mov_b32_e32 v7, v225
	v_mov_b32_e32 v8, v226
	v_mov_b32_e32 v9, v227
	v_mul_f32_e32 v2, v6, v2
	v_mul_f32_e32 v3, v7, v3
	v_cvt_pk_fp8_f32 v10, v2, v3
	v_mul_f32_e32 v2, v8, v4
	v_mul_f32_e32 v3, v9, v5
	v_cvt_pk_fp8_f32 v10, v2, v3 op_sel:[0,0,1]
	global_store_dword v[36:37], v10, off offset:1792
	v_lshl_add_u64 v[36:37], v[36:37], 0, s[48:49]
	s_cbranch_scc0 .LBB0_1093
; __device__ __forceinline__ u32x4 pack8(f32x4 a, f32x4 b) { u32x4 w; w.x = cvtpk(a[0], a[1]); w.y = cvtpk(a[2], a[3]); w.z = cvtpk(b[0], b[1]); w.w = cvtpk(b[2], b[3]); return w; }
; __global__ void __launch_bounds__(512, 2) mega_fwd(Args args) {
;     ...
;         { const float* p = args.in[I_P];
;           for (int i = cx * 512 + tid; i < T * 256 / 8; i += Gc * 512) { const f32x4 a = *(const f32x4*)(p + (size_t)i * 8), b = *(const f32x4*)(p + (size_t)i * 8 + 4); *(u32x4*)(PB + (size_t)i * 8) = pg8::pack8(a, b); } }
.LBB0_1094:
	s_mov_b32 s3, 0x80000
	v_cmp_gt_i32_e32 vcc, s3, v22
	s_and_saveexec_b64 s[4:5], vcc
	v_readlane_b32 s92, v252, 4
	v_readlane_b32 s93, v252, 5
	s_cbranch_execz .LBB0_1097
	v_lshlrev_b64 v[2:3], 5, v[22:23]
	s_waitcnt lgkmcnt(0)
	v_lshl_add_u64 v[2:3], s[8:9], 0, v[2:3]
	s_ashr_i32 s7, s6, 31
	v_lshl_add_u64 v[4:5], v[22:23], 4, s[18:19]
	s_mov_b64 s[10:11], 0x800000
	v_lshl_add_u64 v[2:3], v[2:3], 0, 16
	s_lshl_b64 s[8:9], s[6:7], 5
	v_lshl_add_u64 v[4:5], v[4:5], 0, s[10:11]
	s_lshl_b64 s[10:11], s[6:7], 4
	s_mov_b64 s[42:43], 0
	s_mov_b32 s3, 0x7ffff
	v_mov_b32_e32 v6, v22
	s_mov_b64 s[98:99], exec
	v_mov_b32_e32 v144, v2
	v_mov_b32_e32 v145, v3
	v_mov_b32_e32 v146, v6
	global_load_dwordx4 v[24:27], v[2:3], off offset:-16
	global_load_dwordx4 v[28:31], v[2:3], off
	v_add_u32_e32 v6, s6, v6
	v_lshl_add_u64 v[2:3], v[2:3], 0, s[8:9]
	v_cmp_ge_i32_e32 vcc, s3, v6
	s_nop 1
	s_and_b64 exec, exec, vcc
	global_load_dwordx4 v[32:35], v[2:3], off offset:-16
	global_load_dwordx4 v[36:39], v[2:3], off
	v_add_u32_e32 v6, s6, v6
	v_lshl_add_u64 v[2:3], v[2:3], 0, s[8:9]
	v_cmp_ge_i32_e32 vcc, s3, v6
	s_nop 1
	s_and_b64 exec, exec, vcc
	global_load_dwordx4 v[40:43], v[2:3], off offset:-16
	global_load_dwordx4 v[44:47], v[2:3], off
	v_add_u32_e32 v6, s6, v6
	v_lshl_add_u64 v[2:3], v[2:3], 0, s[8:9]
	v_cmp_ge_i32_e32 vcc, s3, v6
	s_nop 1
	s_and_b64 exec, exec, vcc
	global_load_dwordx4 v[48:51], v[2:3], off offset:-16
	global_load_dwordx4 v[52:55], v[2:3], off
	v_add_u32_e32 v6, s6, v6
	v_lshl_add_u64 v[2:3], v[2:3], 0, s[8:9]
	v_cmp_ge_i32_e32 vcc, s3, v6
	s_nop 1
	s_and_b64 exec, exec, vcc
	global_load_dwordx4 v[56:59], v[2:3], off offset:-16
	global_load_dwordx4 v[60:63], v[2:3], off
	v_add_u32_e32 v6, s6, v6
	v_lshl_add_u64 v[2:3], v[2:3], 0, s[8:9]
	v_cmp_ge_i32_e32 vcc, s3, v6
	s_nop 1
	s_and_b64 exec, exec, vcc
	global_load_dwordx4 v[64:67], v[2:3], off offset:-16
	global_load_dwordx4 v[140:143], v[2:3], off
	s_mov_b64 exec, s[98:99]
	v_mov_b32_e32 v6, v146
	s_waitcnt vmcnt(0)
	v_cvt_pk_bf16_f32 v8, v24, v25
	v_cvt_pk_bf16_f32 v9, v26, v27
	v_cvt_pk_bf16_f32 v10, v28, v29
	v_cvt_pk_bf16_f32 v11, v30, v31
	global_store_dwordx4 v[4:5], v[8:11], off
	s_nop 1
	v_add_u32_e32 v6, s6, v6
	v_lshl_add_u64 v[4:5], v[4:5], 0, s[10:11]
	v_cmp_ge_i32_e32 vcc, s3, v6
	s_nop 1
	s_and_b64 exec, exec, vcc
	v_cvt_pk_bf16_f32 v8, v32, v33
	v_cvt_pk_bf16_f32 v9, v34, v35
	v_cvt_pk_bf16_f32 v10, v36, v37
	v_cvt_pk_bf16_f32 v11, v38, v39
	global_store_dwordx4 v[4:5], v[8:11], off
	s_nop 1
	v_add_u32_e32 v6, s6, v6
	v_lshl_add_u64 v[4:5], v[4:5], 0, s[10:11]
	v_cmp_ge_i32_e32 vcc, s3, v6
	s_nop 1
	s_and_b64 exec, exec, vcc
	v_cvt_pk_bf16_f32 v8, v40, v41
	v_cvt_pk_bf16_f32 v9, v42, v43
	v_cvt_pk_bf16_f32 v10, v44, v45
	v_cvt_pk_bf16_f32 v11, v46, v47
	global_store_dwordx4 v[4:5], v[8:11], off
	s_nop 1
	v_add_u32_e32 v6, s6, v6
	v_lshl_add_u64 v[4:5], v[4:5], 0, s[10:11]
	v_cmp_ge_i32_e32 vcc, s3, v6
	s_nop 1
	s_and_b64 exec, exec, vcc
	v_cvt_pk_bf16_f32 v8, v48, v49
	v_cvt_pk_bf16_f32 v9, v50, v51
	v_cvt_pk_bf16_f32 v10, v52, v53
	v_cvt_pk_bf16_f32 v11, v54, v55
	global_store_dwordx4 v[4:5], v[8:11], off
	s_nop 1
	v_add_u32_e32 v6, s6, v6
	v_lshl_add_u64 v[4:5], v[4:5], 0, s[10:11]
	v_cmp_ge_i32_e32 vcc, s3, v6
	s_nop 1
	s_and_b64 exec, exec, vcc
	v_cvt_pk_bf16_f32 v8, v56, v57
	v_cvt_pk_bf16_f32 v9, v58, v59
	v_cvt_pk_bf16_f32 v10, v60, v61
	v_cvt_pk_bf16_f32 v11, v62, v63
	global_store_dwordx4 v[4:5], v[8:11], off
	s_nop 1
	v_add_u32_e32 v6, s6, v6
	v_lshl_add_u64 v[4:5], v[4:5], 0, s[10:11]
	v_cmp_ge_i32_e32 vcc, s3, v6
	s_nop 1
	s_and_b64 exec, exec, vcc
	v_cvt_pk_bf16_f32 v8, v64, v65
	v_cvt_pk_bf16_f32 v9, v66, v67
	v_cvt_pk_bf16_f32 v10, v140, v141
	v_cvt_pk_bf16_f32 v11, v142, v143
	global_store_dwordx4 v[4:5], v[8:11], off
	s_nop 1
	v_add_u32_e32 v6, s6, v6
	v_lshl_add_u64 v[4:5], v[4:5], 0, s[10:11]
	v_lshl_add_u64 v[2:3], v[2:3], 0, s[8:9]
	v_cmp_ge_i32_e32 vcc, s3, v6
	s_nop 1
	s_and_b64 exec, exec, vcc
	s_cbranch_execz .Lpb_done

; __device__ __forceinline__ unsigned cvtpk(float lo, float hi) { unsigned r; asm volatile("v_cvt_pk_bf16_f32 %0, %1, %2" : "=v"(r) : "v"(lo), "v"(hi)); return r; }
; __device__ __forceinline__ float bf2f(unsigned short b) { return __uint_as_float(((unsigned)b) << 16); }
; __global__ void __launch_bounds__(512, 2) mega_fwd(Args args) {
;     ...
;         { const float* wr_ = args.in[I_W_ROUTER]; bf16_t* WRH = (bf16_t*)(ws + WS_WRH); bf16_t* WRL = (bf16_t*)(ws + WS_WRL);
;           for (int i = cx * 512 + tid; i < NE * DM; i += Gc * 512) { const int e = i >> 11, k = i & (DM - 1); const float w = wr_[(size_t)k * NE + e];
;               const unsigned h = cvtpk(w, 0.f) & 0xffffu; WRH[i] = (bf16_t)h; WRL[i] = (bf16_t)(cvtpk(w - bf2f((bf16_t)h), 0.f) & 0xffffu); } }
.Lpb_done:
.LBB0_1097:
	s_or_b64 exec, exec, s[4:5]
	s_mov_b32 s3, 0x10000
	v_cmp_gt_i32_e32 vcc, s3, v22
	s_and_saveexec_b64 s[4:5], vcc
	s_cbranch_execz .LBB0_1100
	v_lshl_add_u64 v[2:3], v[22:23], 1, s[18:19]
	s_waitcnt lgkmcnt(0)
	s_mov_b64 s[8:9], 0x280000
	s_ashr_i32 s7, s6, 31
	v_lshl_add_u64 v[2:3], v[2:3], 0, s[8:9]
	s_lshl_b64 s[8:9], s[6:7], 1
	s_lshl_b32 s3, s82, 14
	s_lshl_b32 s7, s87, 14
	v_lshlrev_b32_e32 v6, 5, v22
	s_sub_i32 s3, s3, s7
	s_mov_b64 s[10:11], 0
	v_mov_b32_e32 v5, 0
	s_mov_b32 s7, 0xffff
	v_mov_b32_e32 v7, v22
